# combine phase: the four gathered expert rows and the residual row of both tokens of an iteration are requested together (one memory round trip per token pair instead of four per token)
# speedup vs baseline: 1.0107x; 1.0086x over previous
; DI void phase_combine(const Frame& F, int l) {
;     ...
;         const int ev = tok_e[(size_t)t0 * 4 + F.lane]; const int slotv = pstart[ev] + tok_p[(size_t)t0 * 4 + F.lane]; const int gvi = __builtin_bit_cast(int, tok_g[(size_t)t0 * 4 + F.lane]);
; #pragma unroll 2
;         for (int q = 0; q < 16; ++q) { const int t = t0 + q;
;             f32x4 y[4], x[4], hv[4];
; #pragma unroll
;             for (int j = 0; j < 4; ++j) y[j] = (f32x4){0.f, 0.f, 0.f, 0.f};
;             load_bf16_row((const bf16_t*)(F.ws + WS_XB) + (size_t)t * D, F.lane, x);
; #pragma unroll
;             for (int k = 0; k < 4; ++k) { const int slot = __builtin_amdgcn_readlane(slotv, 4 * q + k); const float gk = __builtin_bit_cast(float, __builtin_amdgcn_readlane(gvi, 4 * q + k)) * ysc;
;                 const unsigned char* rp = (const unsigned char*)(F.ws + WS_XS) + (size_t)slot * D + 8 * F.lane; unsigned w[4];
; #pragma unroll
;                 for (int g = 0; g < 2; ++g) { const u32x2 ww = *(const u32x2*)(rp + 512 * g); w[2 * g] = ww.x; w[2 * g + 1] = ww.y; }
; #pragma unroll
;                 for (int j = 0; j < 4; ++j) { const f32x2 lo = __builtin_amdgcn_cvt_pk_f32_fp8((int)w[j], false), hi = __builtin_amdgcn_cvt_pk_f32_fp8((int)w[j], true); y[j] += (f32x4){lo.x, lo.y, hi.x, hi.y} * gk; } }
.LBB0_1391:
	s_ashr_i32 s55, s54, 31
	s_lshl_b64 s[4:5], s[54:55], 11
	s_add_i32 s2, s22, -7
	v_lshl_add_u64 v[74:75], v[68:69], 0, s[4:5]
	v_readlane_b32 s4, v99, s2
	s_ashr_i32 s5, s4, 31
	s_lshl_b64 s[4:5], s[4:5], 10
	v_lshl_add_u64 v[76:77], v[70:71], 0, s[4:5]
	global_load_dwordx4 v[52:55], v[74:75], off
	global_load_dwordx4 v[60:63], v[74:75], off offset:1024
	global_load_dwordx2 v[78:79], v[76:77], off
	s_nop 0
	global_load_dwordx2 v[76:77], v[76:77], off offset:512
	s_add_i32 s66, s22, -6
	v_readlane_b32 s68, v99, s66
	s_ashr_i32 s69, s68, 31
	s_lshl_b64 s[68:69], s[68:69], 10
	v_lshl_add_u64 v[162:163], v[70:71], 0, s[68:69]
	global_load_dwordx2 v[150:151], v[162:163], off
	global_load_dwordx2 v[152:153], v[162:163], off offset:512
	s_add_i32 s66, s22, -5
	v_readlane_b32 s68, v99, s66
	s_ashr_i32 s69, s68, 31
	s_lshl_b64 s[68:69], s[68:69], 10
	v_lshl_add_u64 v[164:165], v[70:71], 0, s[68:69]
	global_load_dwordx2 v[154:155], v[164:165], off
	global_load_dwordx2 v[156:157], v[164:165], off offset:512
	s_add_i32 s66, s22, -4
	v_readlane_b32 s68, v99, s66
	s_ashr_i32 s69, s68, 31
	s_lshl_b64 s[68:69], s[68:69], 10
	v_lshl_add_u64 v[166:167], v[70:71], 0, s[68:69]
	global_load_dwordx2 v[158:159], v[166:167], off
	global_load_dwordx2 v[160:161], v[166:167], off offset:512
	s_add_i32 s66, s54, 1
	s_ashr_i32 s67, s66, 31
	s_lshl_b64 s[66:67], s[66:67], 11
	v_lshl_add_u64 v[144:145], v[68:69], 0, s[66:67]
	global_load_dwordx4 v[168:171], v[144:145], off
	global_load_dwordx4 v[172:175], v[144:145], off offset:1024
	s_add_i32 s66, s22, -3
	v_readlane_b32 s68, v99, s66
	s_ashr_i32 s69, s68, 31
	s_lshl_b64 s[68:69], s[68:69], 10
	v_lshl_add_u64 v[146:147], v[70:71], 0, s[68:69]
	global_load_dwordx2 v[176:177], v[146:147], off
	global_load_dwordx2 v[178:179], v[146:147], off offset:512
	s_add_i32 s66, s22, -2
	v_readlane_b32 s68, v99, s66
	s_ashr_i32 s69, s68, 31
	s_lshl_b64 s[68:69], s[68:69], 10
	v_lshl_add_u64 v[146:147], v[70:71], 0, s[68:69]
	global_load_dwordx2 v[180:181], v[146:147], off
	global_load_dwordx2 v[182:183], v[146:147], off offset:512
	s_add_i32 s66, s22, -1
	v_readlane_b32 s68, v99, s66
	s_ashr_i32 s69, s68, 31
	s_lshl_b64 s[68:69], s[68:69], 10
	v_lshl_add_u64 v[146:147], v[70:71], 0, s[68:69]
	global_load_dwordx2 v[184:185], v[146:147], off
	global_load_dwordx2 v[186:187], v[146:147], off offset:512
	s_add_i32 s66, s22, 0
	v_readlane_b32 s68, v99, s66
	s_ashr_i32 s69, s68, 31
	s_lshl_b64 s[68:69], s[68:69], 10
	v_lshl_add_u64 v[146:147], v[70:71], 0, s[68:69]
	global_load_dwordx2 v[188:189], v[146:147], off
	global_load_dwordx2 v[190:191], v[146:147], off offset:512
	s_waitcnt vmcnt(20)
	v_readlane_b32 s2, v98, s2
	s_lshl_b64 s[56:57], s[54:55], 10
	s_and_b64 vcc, exec, s[46:47]
	v_mul_f32_e32 v80, s2, v65
	s_add_i32 s2, s22, -6
	v_readlane_b32 s4, v99, s2
	s_ashr_i32 s5, s4, 31
	s_lshl_b64 s[4:5], s[4:5], 10
	v_readlane_b32 s2, v98, s2
	s_waitcnt vmcnt(19)
	v_lshlrev_b32_e32 v48, 16, v52
	s_waitcnt vmcnt(17)
	v_cvt_pk_f32_fp8_e32 v[82:83], v78
	v_cvt_pk_f32_fp8_sdwa v[84:85], v78 src0_sel:WORD_1
	v_cvt_pk_f32_fp8_e32 v[86:87], v79
	v_cvt_pk_f32_fp8_sdwa v[78:79], v79 src0_sel:WORD_1
	s_waitcnt vmcnt(16)
	v_cvt_pk_f32_fp8_e32 v[88:89], v76
	v_cvt_pk_f32_fp8_sdwa v[90:91], v76 src0_sel:WORD_1
	v_cvt_pk_f32_fp8_e32 v[92:93], v77
	v_cvt_pk_f32_fp8_sdwa v[76:77], v77 src0_sel:WORD_1
	v_pk_fma_f32 v[84:85], v[80:81], v[84:85], 0 op_sel_hi:[0,1,0]
	v_pk_fma_f32 v[82:83], v[80:81], v[82:83], 0 op_sel_hi:[0,1,0]
	v_pk_fma_f32 v[78:79], v[80:81], v[78:79], 0 op_sel_hi:[0,1,0]
	v_pk_fma_f32 v[86:87], v[80:81], v[86:87], 0 op_sel_hi:[0,1,0]
	v_pk_fma_f32 v[88:89], v[80:81], v[88:89], 0 op_sel_hi:[0,1,0]
	v_pk_fma_f32 v[90:91], v[80:81], v[90:91], 0 op_sel_hi:[0,1,0]
	v_pk_fma_f32 v[92:93], v[80:81], v[92:93], 0 op_sel_hi:[0,1,0]
	v_pk_fma_f32 v[76:77], v[80:81], v[76:77], 0 op_sel_hi:[0,1,0]
	v_lshl_add_u64 v[80:81], v[70:71], 0, s[4:5]
	s_nop 0
	v_mul_f32_e32 v100, s2, v65
	s_add_i32 s2, s22, -5
	v_readlane_b32 s4, v99, s2
	s_ashr_i32 s5, s4, 31
	s_lshl_b64 s[4:5], s[4:5], 10
	v_readlane_b32 s2, v98, s2
	v_and_b32_e32 v49, 0xffff0000, v52
	v_lshlrev_b32_e32 v50, 16, v53
	v_mul_f32_e32 v106, s2, v65
	s_add_i32 s2, s22, -4
	v_and_b32_e32 v51, 0xffff0000, v53
	v_lshlrev_b32_e32 v52, 16, v54
	v_and_b32_e32 v53, 0xffff0000, v54
	v_lshlrev_b32_e32 v54, 16, v55
	v_and_b32_e32 v55, 0xffff0000, v55
	v_lshlrev_b32_e32 v56, 16, v60
	v_and_b32_e32 v57, 0xffff0000, v60
	v_lshlrev_b32_e32 v58, 16, v61
	v_and_b32_e32 v59, 0xffff0000, v61
	v_lshlrev_b32_e32 v60, 16, v62
	v_and_b32_e32 v61, 0xffff0000, v62
	v_lshlrev_b32_e32 v62, 16, v63
	v_and_b32_e32 v63, 0xffff0000, v63
	s_waitcnt vmcnt(15)
	v_cvt_pk_f32_fp8_e32 v[102:103], v150
	v_cvt_pk_f32_fp8_sdwa v[104:105], v150 src0_sel:WORD_1
	v_pk_fma_f32 v[82:83], v[100:101], v[102:103], v[82:83] op_sel_hi:[0,1,1]
	v_cvt_pk_f32_fp8_e32 v[102:103], v151
	v_cvt_pk_f32_fp8_sdwa v[94:95], v151 src0_sel:WORD_1
	v_pk_fma_f32 v[84:85], v[100:101], v[104:105], v[84:85] op_sel_hi:[0,1,1]
	v_pk_fma_f32 v[86:87], v[100:101], v[102:103], v[86:87] op_sel_hi:[0,1,1]
	v_pk_fma_f32 v[78:79], v[100:101], v[94:95], v[78:79] op_sel_hi:[0,1,1]
	s_waitcnt vmcnt(14)
	v_cvt_pk_f32_fp8_e32 v[94:95], v152
	v_cvt_pk_f32_fp8_sdwa v[102:103], v152 src0_sel:WORD_1
	v_pk_fma_f32 v[94:95], v[100:101], v[94:95], v[88:89] op_sel_hi:[0,1,1]
	v_cvt_pk_f32_fp8_e32 v[88:89], v153
	v_cvt_pk_f32_fp8_sdwa v[80:81], v153 src0_sel:WORD_1
	v_pk_fma_f32 v[102:103], v[100:101], v[102:103], v[90:91] op_sel_hi:[0,1,1]
	v_pk_fma_f32 v[104:105], v[100:101], v[80:81], v[76:77] op_sel_hi:[0,1,1]
	v_lshl_add_u64 v[80:81], v[70:71], 0, s[4:5]
	v_pk_fma_f32 v[76:77], v[100:101], v[88:89], v[92:93] op_sel_hi:[0,1,1]
	v_readlane_b32 s4, v99, s2
	s_ashr_i32 s5, s4, 31
	s_lshl_b64 s[4:5], s[4:5], 10
	v_readlane_b32 s2, v98, s2
	s_waitcnt vmcnt(13)
; DI void phase_combine(const Frame& F, int l) {
;     ...
;             for (int k = 0; k < 4; ++k) { const int slot = __builtin_amdgcn_readlane(slotv, 4 * q + k); const float gk = __builtin_bit_cast(float, __builtin_amdgcn_readlane(gvi, 4 * q + k)) * ysc;
;                 const unsigned char* rp = (const unsigned char*)(F.ws + WS_XS) + (size_t)slot * D + 8 * F.lane; unsigned w[4];
; #pragma unroll
;                 for (int g = 0; g < 2; ++g) { const u32x2 ww = *(const u32x2*)(rp + 512 * g); w[2 * g] = ww.x; w[2 * g + 1] = ww.y; }
; #pragma unroll
;                 for (int j = 0; j < 4; ++j) { const f32x2 lo = __builtin_amdgcn_cvt_pk_f32_fp8((int)w[j], false), hi = __builtin_amdgcn_cvt_pk_f32_fp8((int)w[j], true); y[j] += (f32x4){lo.x, lo.y, hi.x, hi.y} * gk; } }
;             const float rstd = rms_rstd(y);
; #pragma unroll
;             for (int j = 0; j < 4; ++j) x[j] = x[j] + Bv[j] * (y[j] * rstd);
	v_cvt_pk_f32_fp8_e32 v[80:81], v154
	v_cvt_pk_f32_fp8_sdwa v[88:89], v154 src0_sel:WORD_1
	v_pk_fma_f32 v[90:91], v[106:107], v[80:81], v[82:83] op_sel_hi:[0,1,1]
	v_cvt_pk_f32_fp8_sdwa v[82:83], v155 src0_sel:WORD_1
	v_pk_fma_f32 v[88:89], v[106:107], v[88:89], v[84:85] op_sel_hi:[0,1,1]
	v_cvt_pk_f32_fp8_e32 v[80:81], v155
	s_waitcnt vmcnt(12)
	v_cvt_pk_f32_fp8_sdwa v[92:93], v157 src0_sel:WORD_1
	v_pk_fma_f32 v[84:85], v[106:107], v[82:83], v[78:79] op_sel_hi:[0,1,1]
	v_cvt_pk_f32_fp8_e32 v[78:79], v156
	v_pk_fma_f32 v[86:87], v[106:107], v[80:81], v[86:87] op_sel_hi:[0,1,1]
	v_cvt_pk_f32_fp8_sdwa v[82:83], v156 src0_sel:WORD_1
	v_mul_f32_e32 v100, s2, v65
	v_pk_fma_f32 v[80:81], v[106:107], v[78:79], v[94:95] op_sel_hi:[0,1,1]
	v_cvt_pk_f32_fp8_e32 v[78:79], v157
	v_pk_fma_f32 v[82:83], v[106:107], v[82:83], v[102:103] op_sel_hi:[0,1,1]
	v_pk_fma_f32 v[76:77], v[106:107], v[78:79], v[76:77] op_sel_hi:[0,1,1]
	v_pk_fma_f32 v[78:79], v[106:107], v[92:93], v[104:105] op_sel_hi:[0,1,1]
	v_lshl_add_u64 v[92:93], v[70:71], 0, s[4:5]
	s_nop 0
	s_waitcnt vmcnt(11)
	v_cvt_pk_f32_fp8_e32 v[102:103], v158
	v_cvt_pk_f32_fp8_sdwa v[104:105], v158 src0_sel:WORD_1
	v_pk_fma_f32 v[90:91], v[100:101], v[102:103], v[90:91] op_sel_hi:[0,1,1]
	v_cvt_pk_f32_fp8_e32 v[102:103], v159
	v_cvt_pk_f32_fp8_sdwa v[94:95], v159 src0_sel:WORD_1
	v_pk_fma_f32 v[88:89], v[100:101], v[104:105], v[88:89] op_sel_hi:[0,1,1]
	v_pk_fma_f32 v[86:87], v[100:101], v[102:103], v[86:87] op_sel_hi:[0,1,1]
	v_pk_fma_f32 v[84:85], v[100:101], v[94:95], v[84:85] op_sel_hi:[0,1,1]
	s_waitcnt vmcnt(10)
	v_cvt_pk_f32_fp8_e32 v[94:95], v160
	v_cvt_pk_f32_fp8_sdwa v[102:103], v160 src0_sel:WORD_1
	v_pk_fma_f32 v[80:81], v[100:101], v[94:95], v[80:81] op_sel_hi:[0,1,1]
	v_cvt_pk_f32_fp8_e32 v[94:95], v161
	v_cvt_pk_f32_fp8_sdwa v[92:93], v161 src0_sel:WORD_1
	v_pk_fma_f32 v[82:83], v[100:101], v[102:103], v[82:83] op_sel_hi:[0,1,1]
	v_pk_fma_f32 v[76:77], v[100:101], v[94:95], v[76:77] op_sel_hi:[0,1,1]
	v_pk_fma_f32 v[78:79], v[100:101], v[92:93], v[78:79] op_sel_hi:[0,1,1]
	v_pk_mul_f32 v[92:93], v[88:89], v[88:89]
	v_pk_mul_f32 v[94:95], v[90:91], v[90:91]
	s_nop 0
	v_pk_mov_b32 v[100:101], v[94:95], v[92:93] op_sel:[1,0]
	v_mov_b32_e32 v95, v93
	v_pk_add_f32 v[92:93], v[100:101], v[94:95]
	v_pk_mul_f32 v[94:95], v[84:85], v[84:85]
	v_pk_mul_f32 v[100:101], v[86:87], v[86:87]
	v_pk_add_f32 v[92:93], v[92:93], v[92:93] op_sel:[0,1] op_sel_hi:[1,0]
	v_pk_mov_b32 v[102:103], v[100:101], v[94:95] op_sel:[1,0]
	v_mov_b32_e32 v101, v95
	v_pk_add_f32 v[94:95], v[102:103], v[100:101]
	v_mul_f32_e32 v100, v76, v76
	v_mul_f32_e32 v101, v77, v77
	v_pk_add_f32 v[94:95], v[94:95], v[94:95] op_sel:[0,1] op_sel_hi:[1,0]
	v_mov_b32_e32 v93, v100
	v_mov_b32_e32 v95, v101
	v_pk_add_f32 v[92:93], v[92:93], v[94:95]
	v_mul_f32_e32 v94, v81, v81
	v_mul_f32_e32 v100, v83, v83
	v_mul_f32_e32 v102, v78, v78
	v_mul_f32_e32 v103, v79, v79
	v_pk_fma_f32 v[94:95], v[80:81], v[80:81], v[94:95] op_sel_hi:[1,1,0]
	v_pk_fma_f32 v[100:101], v[82:83], v[82:83], v[100:101] op_sel_hi:[1,1,0]
	v_mov_b32_e32 v95, v102
	v_mov_b32_e32 v101, v103
	v_pk_add_f32 v[94:95], v[94:95], v[100:101]
	s_nop 0
	v_pk_add_f32 v[92:93], v[92:93], v[94:95]
	s_nop 0
	v_add_f32_e32 v92, v92, v93
	s_nop 1
	v_add_f32_dpp v92, v92, v92 quad_perm:[1,0,3,2] row_mask:0xf bank_mask:0xf bound_ctrl:1
	s_nop 1
	v_add_f32_dpp v92, v92, v92 quad_perm:[2,3,0,1] row_mask:0xf bank_mask:0xf bound_ctrl:1
	s_nop 1
	v_add_f32_dpp v92, v92, v92 row_half_mirror row_mask:0xf bank_mask:0xf bound_ctrl:1
	s_nop 1
	v_add_f32_dpp v92, v92, v92 row_mirror row_mask:0xf bank_mask:0xf bound_ctrl:1
	s_nop 0
	v_readlane_b32 s2, v92, 16
	v_readlane_b32 s10, v92, 48
	v_readlane_b32 s4, v92, 0
	v_readlane_b32 s5, v92, 32
	v_mov_b32_e32 v92, s2
	v_mov_b32_e32 v93, s10
	v_pk_add_f32 v[92:93], s[4:5], v[92:93]
	s_mov_b64 s[4:5], -1
	v_add_f32_e32 v92, v92, v93
	v_mov_b32_e32 v93, 0x358637bd
	s_nop 0
	v_fmac_f32_e32 v93, 0x3a800000, v92
	v_rsq_f32_e32 v92, v93
	s_nop 0
	v_pk_mul_f32 v[90:91], v[90:91], v[92:93] op_sel_hi:[1,0]
	v_pk_mul_f32 v[88:89], v[88:89], v[92:93] op_sel_hi:[1,0]
	v_pk_mul_f32 v[86:87], v[86:87], v[92:93] op_sel_hi:[1,0]
	v_pk_mul_f32 v[84:85], v[84:85], v[92:93] op_sel_hi:[1,0]
	v_pk_mul_f32 v[80:81], v[80:81], v[92:93] op_sel_hi:[1,0]
	v_pk_mul_f32 v[82:83], v[82:83], v[92:93] op_sel_hi:[1,0]
	v_pk_mul_f32 v[76:77], v[76:77], v[92:93] op_sel_hi:[1,0]
	v_pk_mul_f32 v[78:79], v[78:79], v[92:93] op_sel_hi:[1,0]
	v_pk_fma_f32 v[50:51], v[2:3], v[88:89], v[50:51]
	v_pk_fma_f32 v[48:49], v[0:1], v[90:91], v[48:49]
	v_pk_fma_f32 v[54:55], v[6:7], v[84:85], v[54:55]
	v_pk_fma_f32 v[52:53], v[4:5], v[86:87], v[52:53]
	v_pk_fma_f32 v[58:59], v[10:11], v[82:83], v[58:59]
	v_pk_fma_f32 v[56:57], v[8:9], v[80:81], v[56:57]
	v_pk_fma_f32 v[62:63], v[14:15], v[78:79], v[62:63]
	v_pk_fma_f32 v[60:61], v[12:13], v[76:77], v[60:61]
	s_cbranch_vccz .LBB0_1393
; DI unsigned pk2(float lo, float hi) { return f2bf(lo) | (f2bf(hi) << 16); }
; DI unsigned pk_fp8x4(float a, float b, float c, float d) { int p = 0; p = __builtin_amdgcn_cvt_pk_fp8_f32(a, b, p, false); p = __builtin_amdgcn_cvt_pk_fp8_f32(c, d, p, true); return (unsigned)p; }
; DI void mod_norm_row8(const f32x4 (&x)[4], const f32x4 (&A)[4], const f32x4 (&S)[4], unsigned char* orow, int lane) {
;     const float rstd = rms_rstd(x);
; #pragma unroll
;     for (int g = 0; g < 2; ++g) { const f32x4 h0 = x[2 * g] * rstd * A[2 * g] + S[2 * g], h1 = x[2 * g + 1] * rstd * A[2 * g + 1] + S[2 * g + 1];
;         u32x2 w; w.x = pk_fp8x4(h0.x, h0.y, h0.z, h0.w); w.y = pk_fp8x4(h1.x, h1.y, h1.z, h1.w); *(u32x2*)(orow + 8 * lane + 512 * g) = w; }
; }
; DI void store_bf16_row(bf16_t* row, int lane, const f32x4 (&v)[4]) {
; #pragma unroll
;     for (int g = 0; g < 2; ++g) { u32x4 w; w.x = pk2(v[2 * g].x, v[2 * g].y); w.y = pk2(v[2 * g].z, v[2 * g].w); w.z = pk2(v[2 * g + 1].x, v[2 * g + 1].y); w.w = pk2(v[2 * g + 1].z, v[2 * g + 1].w);
;         *(u32x4*)(row + 8 * lane + 512 * g) = w; }
; DI void phase_combine(const Frame& F, int l) {
;     ...
;             if (more) { store_bf16_row((bf16_t*)(F.ws + WS_XB) + (size_t)t * D, F.lane, x); mod_norm_row8(x, Av, Sv, (unsigned char*)(F.ws + WS_H8) + (size_t)t * D, F.lane); }
	v_bfe_u32 v76, v48, 16, 1
	v_add3_u32 v76, v48, v76, s15
	v_bfe_u32 v77, v49, 16, 1
	v_lshrrev_b32_e32 v76, 16, v76
	v_add3_u32 v77, v49, v77, s15
	v_and_or_b32 v76, v77, s16, v76
	v_bfe_u32 v77, v50, 16, 1
	v_add3_u32 v77, v50, v77, s15
	v_bfe_u32 v78, v51, 16, 1
	v_lshrrev_b32_e32 v77, 16, v77
	v_add3_u32 v78, v51, v78, s15
	v_and_or_b32 v77, v78, s16, v77
	v_bfe_u32 v78, v52, 16, 1
	v_add3_u32 v78, v52, v78, s15
	v_bfe_u32 v79, v53, 16, 1
	v_lshrrev_b32_e32 v78, 16, v78
	v_add3_u32 v79, v53, v79, s15
	v_and_or_b32 v78, v79, s16, v78
	v_bfe_u32 v79, v54, 16, 1
	v_add3_u32 v79, v54, v79, s15
	v_bfe_u32 v80, v55, 16, 1
	v_lshrrev_b32_e32 v79, 16, v79
	v_add3_u32 v80, v55, v80, s15
	v_and_or_b32 v79, v80, s16, v79
	global_store_dwordx4 v[74:75], v[76:79], off
	v_bfe_u32 v80, v63, 16, 1
	v_add3_u32 v80, v63, v80, s15
	v_bfe_u32 v76, v56, 16, 1
	v_add3_u32 v76, v56, v76, s15
	v_bfe_u32 v77, v57, 16, 1
	v_lshrrev_b32_e32 v76, 16, v76
	v_add3_u32 v77, v57, v77, s15
	v_and_or_b32 v76, v77, s16, v76
	v_bfe_u32 v77, v58, 16, 1
	v_add3_u32 v77, v58, v77, s15
	v_bfe_u32 v78, v59, 16, 1
	v_lshrrev_b32_e32 v77, 16, v77
	v_add3_u32 v78, v59, v78, s15
	v_and_or_b32 v77, v78, s16, v77
	v_bfe_u32 v78, v60, 16, 1
	v_add3_u32 v78, v60, v78, s15
	v_bfe_u32 v79, v61, 16, 1
	v_lshrrev_b32_e32 v78, 16, v78
	v_add3_u32 v79, v61, v79, s15
	v_and_or_b32 v78, v79, s16, v78
	v_bfe_u32 v79, v62, 16, 1
	v_add3_u32 v79, v62, v79, s15
	v_lshrrev_b32_e32 v79, 16, v79
	v_and_or_b32 v79, v80, s16, v79
	global_store_dwordx4 v[74:75], v[76:79], off offset:1024
	v_pk_mul_f32 v[74:75], v[50:51], v[50:51]
	v_mov_b32_e32 v83, v193
	v_pk_mul_f32 v[76:77], v[48:49], v[48:49]
	v_mov_b32_e32 v82, v193
	v_pk_mov_b32 v[78:79], v[76:77], v[74:75] op_sel:[1,0]
	v_mov_b32_e32 v77, v75
	v_pk_add_f32 v[74:75], v[78:79], v[76:77]
	v_pk_mul_f32 v[76:77], v[54:55], v[54:55]
	v_pk_add_f32 v[74:75], v[74:75], v[74:75] op_sel_hi:[0,1]
	v_pk_mul_f32 v[78:79], v[52:53], v[52:53]
	v_mul_f32_e32 v74, v56, v56
	v_pk_mov_b32 v[80:81], v[78:79], v[76:77] op_sel:[1,0]
	v_mov_b32_e32 v79, v77
	v_pk_add_f32 v[76:77], v[80:81], v[78:79]
	v_pk_fma_f32 v[78:79], v[56:57], v[56:57], v[74:75] op_sel_hi:[1,1,0]
	v_mul_f32_e32 v74, v58, v58
	v_pk_add_f32 v[76:77], v[76:77], v[76:77] op_sel_hi:[0,1]
	v_pk_fma_f32 v[80:81], v[58:59], v[58:59], v[74:75] op_sel_hi:[1,1,0]
	v_mul_f32_e32 v78, v60, v60
	v_mul_f32_e32 v80, v61, v61
	v_mul_f32_e32 v74, v62, v62
	v_mul_f32_e32 v76, v63, v63
	v_pk_add_f32 v[78:79], v[78:79], v[80:81]
	v_pk_add_f32 v[74:75], v[74:75], v[76:77]
	v_mov_b32_e32 v84, v193
	v_pk_add_f32 v[74:75], v[78:79], v[74:75]
	v_mov_b32_e32 v85, v193
	v_add_f32_e32 v74, v74, v75
	s_nop 1
	v_add_f32_dpp v74, v74, v74 quad_perm:[1,0,3,2] row_mask:0xf bank_mask:0xf bound_ctrl:1
	s_nop 1
	v_add_f32_dpp v74, v74, v74 quad_perm:[2,3,0,1] row_mask:0xf bank_mask:0xf bound_ctrl:1
	s_nop 1
	v_add_f32_dpp v74, v74, v74 row_half_mirror row_mask:0xf bank_mask:0xf bound_ctrl:1
	s_nop 1
	v_add_f32_dpp v74, v74, v74 row_mirror row_mask:0xf bank_mask:0xf bound_ctrl:1
	s_nop 0
	v_readlane_b32 s2, v74, 16
	v_readlane_b32 s10, v74, 48
	v_readlane_b32 s4, v74, 0
	v_readlane_b32 s5, v74, 32
	v_mov_b32_e32 v74, s2
	v_mov_b32_e32 v75, s10
	v_pk_add_f32 v[74:75], s[4:5], v[74:75]
	s_mov_b64 s[4:5], 0
	v_add_f32_e32 v74, v74, v75
	v_mov_b32_e32 v75, 0x358637bd
	s_nop 0
	v_fmac_f32_e32 v75, 0x3a800000, v74
	v_rsq_f32_e32 v74, v75
	s_nop 0
	v_pk_mul_f32 v[80:81], v[52:53], v[74:75] op_sel_hi:[1,0]
	s_nop 0
	v_pk_fma_f32 v[80:81], v[36:37], v[80:81], v[16:17]
	v_pk_mul_f32 v[76:77], v[48:49], v[74:75] op_sel_hi:[1,0]
	v_cvt_pk_fp8_f32 v83, v80, v81
	v_pk_fma_f32 v[76:77], v[32:33], v[76:77], v[20:21]
	v_pk_mul_f32 v[80:81], v[60:61], v[74:75] op_sel_hi:[1,0]
	v_cvt_pk_fp8_f32 v82, v76, v77
	v_pk_mul_f32 v[76:77], v[54:55], v[74:75] op_sel_hi:[1,0]
	v_pk_fma_f32 v[80:81], v[44:45], v[80:81], v[24:25]
	v_pk_fma_f32 v[76:77], v[38:39], v[76:77], v[18:19]
	v_pk_mul_f32 v[78:79], v[50:51], v[74:75] op_sel_hi:[1,0]
	v_cvt_pk_fp8_f32 v83, v76, v77 op_sel:[0,0,1]
	v_pk_mul_f32 v[76:77], v[56:57], v[74:75] op_sel_hi:[1,0]
	v_cvt_pk_fp8_f32 v85, v80, v81
	v_pk_fma_f32 v[76:77], v[40:41], v[76:77], v[28:29]
	v_pk_fma_f32 v[78:79], v[34:35], v[78:79], v[22:23]
	v_cvt_pk_fp8_f32 v84, v76, v77
	v_cvt_pk_fp8_f32 v82, v78, v79 op_sel:[0,0,1]
	v_pk_mul_f32 v[78:79], v[58:59], v[74:75] op_sel_hi:[1,0]
	v_pk_mul_f32 v[74:75], v[62:63], v[74:75] op_sel_hi:[1,0]
	v_pk_fma_f32 v[78:79], v[42:43], v[78:79], v[30:31]
	v_pk_fma_f32 v[74:75], v[46:47], v[74:75], v[26:27]
	v_cvt_pk_fp8_f32 v84, v78, v79 op_sel:[0,0,1]
	v_cvt_pk_fp8_f32 v85, v74, v75 op_sel:[0,0,1]
	v_lshl_add_u64 v[74:75], v[72:73], 0, s[56:57]
	global_store_dwordx2 v[74:75], v[82:83], off
	global_store_dwordx2 v[74:75], v[84:85], off offset:512

; DI void phase_combine(const Frame& F, int l) {
;     ...
;         for (int q = 0; q < 16; ++q) { const int t = t0 + q;
;             f32x4 y[4], x[4], hv[4];
; #pragma unroll
;             for (int j = 0; j < 4; ++j) y[j] = (f32x4){0.f, 0.f, 0.f, 0.f};
;             load_bf16_row((const bf16_t*)(F.ws + WS_XB) + (size_t)t * D, F.lane, x);
; #pragma unroll
;             for (int k = 0; k < 4; ++k) { const int slot = __builtin_amdgcn_readlane(slotv, 4 * q + k); const float gk = __builtin_bit_cast(float, __builtin_amdgcn_readlane(gvi, 4 * q + k)) * ysc;
;                 const unsigned char* rp = (const unsigned char*)(F.ws + WS_XS) + (size_t)slot * D + 8 * F.lane; unsigned w[4];
; #pragma unroll
;                 for (int g = 0; g < 2; ++g) { const u32x2 ww = *(const u32x2*)(rp + 512 * g); w[2 * g] = ww.x; w[2 * g + 1] = ww.y; }
; #pragma unroll
;                 for (int j = 0; j < 4; ++j) { const f32x2 lo = __builtin_amdgcn_cvt_pk_f32_fp8((int)w[j], false), hi = __builtin_amdgcn_cvt_pk_f32_fp8((int)w[j], true); y[j] += (f32x4){lo.x, lo.y, hi.x, hi.y} * gk; } }
.LBB0_1395:
	s_add_i32 s4, s54, 1
	s_ashr_i32 s5, s4, 31
	s_lshl_b64 s[56:57], s[4:5], 10
	s_lshl_b64 s[4:5], s[4:5], 11
	s_add_i32 s2, s22, -3
	v_lshl_add_u64 v[74:75], v[68:69], 0, s[4:5]
	v_readlane_b32 s4, v99, s2
	s_ashr_i32 s5, s4, 31
	s_lshl_b64 s[4:5], s[4:5], 10
	v_lshl_add_u64 v[76:77], v[70:71], 0, s[4:5]
	s_nop 0
	s_add_i32 s66, s22, -2
	v_readlane_b32 s68, v99, s66
	s_ashr_i32 s69, s68, 31
	s_lshl_b64 s[68:69], s[68:69], 10
	v_lshl_add_u64 v[162:163], v[70:71], 0, s[68:69]
	s_add_i32 s66, s22, -1
	v_readlane_b32 s68, v99, s66
	s_ashr_i32 s69, s68, 31
	s_lshl_b64 s[68:69], s[68:69], 10
	v_lshl_add_u64 v[164:165], v[70:71], 0, s[68:69]
	s_add_i32 s66, s22, 0
	v_readlane_b32 s68, v99, s66
	s_ashr_i32 s69, s68, 31
	s_lshl_b64 s[68:69], s[68:69], 10
	v_lshl_add_u64 v[166:167], v[70:71], 0, s[68:69]
	v_readlane_b32 s2, v98, s2
	s_and_b64 vcc, exec, s[36:37]
	s_waitcnt vmcnt(0)
	v_lshlrev_b32_e32 v48, 16, v168
	v_mul_f32_e32 v80, s2, v65
	s_waitcnt vmcnt(4)
	v_cvt_pk_f32_fp8_e32 v[82:83], v176
	v_cvt_pk_f32_fp8_sdwa v[84:85], v176 src0_sel:WORD_1
	v_cvt_pk_f32_fp8_e32 v[86:87], v177
	v_cvt_pk_f32_fp8_sdwa v[78:79], v177 src0_sel:WORD_1
	s_waitcnt vmcnt(4)
	v_cvt_pk_f32_fp8_e32 v[88:89], v178
	v_cvt_pk_f32_fp8_sdwa v[90:91], v178 src0_sel:WORD_1
	v_cvt_pk_f32_fp8_e32 v[92:93], v179
	v_cvt_pk_f32_fp8_sdwa v[76:77], v179 src0_sel:WORD_1
	s_add_i32 s2, s22, -2
	v_readlane_b32 s4, v99, s2
	s_ashr_i32 s5, s4, 31
	s_lshl_b64 s[4:5], s[4:5], 10
	v_pk_fma_f32 v[84:85], v[80:81], v[84:85], 0 op_sel_hi:[0,1,0]
	v_pk_fma_f32 v[82:83], v[80:81], v[82:83], 0 op_sel_hi:[0,1,0]
	v_pk_fma_f32 v[78:79], v[80:81], v[78:79], 0 op_sel_hi:[0,1,0]
	v_pk_fma_f32 v[86:87], v[80:81], v[86:87], 0 op_sel_hi:[0,1,0]
	v_pk_fma_f32 v[88:89], v[80:81], v[88:89], 0 op_sel_hi:[0,1,0]
	v_pk_fma_f32 v[90:91], v[80:81], v[90:91], 0 op_sel_hi:[0,1,0]
	v_pk_fma_f32 v[92:93], v[80:81], v[92:93], 0 op_sel_hi:[0,1,0]
	v_pk_fma_f32 v[76:77], v[80:81], v[76:77], 0 op_sel_hi:[0,1,0]
	v_lshl_add_u64 v[80:81], v[70:71], 0, s[4:5]
	s_nop 0
	v_readlane_b32 s2, v98, s2
	v_and_b32_e32 v49, 0xffff0000, v168
	v_lshlrev_b32_e32 v50, 16, v169
	v_mul_f32_e32 v100, s2, v65
	s_add_i32 s2, s22, -1
	v_readlane_b32 s4, v99, s2
	s_ashr_i32 s5, s4, 31
	s_lshl_b64 s[4:5], s[4:5], 10
	v_readlane_b32 s2, v98, s2
	v_and_b32_e32 v51, 0xffff0000, v169
	v_lshlrev_b32_e32 v52, 16, v170
	v_mul_f32_e32 v106, s2, v65
	v_readlane_b32 s2, v98, s22
	v_and_b32_e32 v53, 0xffff0000, v170
	v_lshlrev_b32_e32 v54, 16, v171
	v_and_b32_e32 v55, 0xffff0000, v171
	v_lshlrev_b32_e32 v56, 16, v172
	v_and_b32_e32 v57, 0xffff0000, v172
	v_lshlrev_b32_e32 v58, 16, v173
	v_and_b32_e32 v59, 0xffff0000, v173
	v_lshlrev_b32_e32 v60, 16, v174
	v_and_b32_e32 v61, 0xffff0000, v174
	v_lshlrev_b32_e32 v62, 16, v175
	v_and_b32_e32 v63, 0xffff0000, v175
	s_waitcnt vmcnt(4)
	v_cvt_pk_f32_fp8_e32 v[102:103], v180
	v_cvt_pk_f32_fp8_sdwa v[104:105], v180 src0_sel:WORD_1
	v_pk_fma_f32 v[82:83], v[100:101], v[102:103], v[82:83] op_sel_hi:[0,1,1]
	v_cvt_pk_f32_fp8_e32 v[102:103], v181
	v_cvt_pk_f32_fp8_sdwa v[94:95], v181 src0_sel:WORD_1
	v_pk_fma_f32 v[84:85], v[100:101], v[104:105], v[84:85] op_sel_hi:[0,1,1]
	v_pk_fma_f32 v[86:87], v[100:101], v[102:103], v[86:87] op_sel_hi:[0,1,1]
	v_pk_fma_f32 v[78:79], v[100:101], v[94:95], v[78:79] op_sel_hi:[0,1,1]
	s_waitcnt vmcnt(4)
	v_cvt_pk_f32_fp8_e32 v[94:95], v182
	v_cvt_pk_f32_fp8_sdwa v[102:103], v182 src0_sel:WORD_1
	v_pk_fma_f32 v[94:95], v[100:101], v[94:95], v[88:89] op_sel_hi:[0,1,1]
	v_cvt_pk_f32_fp8_e32 v[88:89], v183
	v_cvt_pk_f32_fp8_sdwa v[80:81], v183 src0_sel:WORD_1
	v_pk_fma_f32 v[102:103], v[100:101], v[102:103], v[90:91] op_sel_hi:[0,1,1]
	v_pk_fma_f32 v[104:105], v[100:101], v[80:81], v[76:77] op_sel_hi:[0,1,1]
	v_lshl_add_u64 v[80:81], v[70:71], 0, s[4:5]
	v_pk_fma_f32 v[76:77], v[100:101], v[88:89], v[92:93] op_sel_hi:[0,1,1]
	v_readlane_b32 s4, v99, s22
	s_ashr_i32 s5, s4, 31
	s_lshl_b64 s[4:5], s[4:5], 10
	s_waitcnt vmcnt(4)
	v_cvt_pk_f32_fp8_e32 v[80:81], v184
	v_cvt_pk_f32_fp8_sdwa v[88:89], v184 src0_sel:WORD_1
	v_pk_fma_f32 v[90:91], v[106:107], v[80:81], v[82:83] op_sel_hi:[0,1,1]
	v_cvt_pk_f32_fp8_sdwa v[82:83], v185 src0_sel:WORD_1
	v_pk_fma_f32 v[88:89], v[106:107], v[88:89], v[84:85] op_sel_hi:[0,1,1]
	v_cvt_pk_f32_fp8_e32 v[80:81], v185
	s_waitcnt vmcnt(4)
; DI void phase_combine(const Frame& F, int l) {
;     ...
;             for (int k = 0; k < 4; ++k) { const int slot = __builtin_amdgcn_readlane(slotv, 4 * q + k); const float gk = __builtin_bit_cast(float, __builtin_amdgcn_readlane(gvi, 4 * q + k)) * ysc;
;                 const unsigned char* rp = (const unsigned char*)(F.ws + WS_XS) + (size_t)slot * D + 8 * F.lane; unsigned w[4];
; #pragma unroll
;                 for (int g = 0; g < 2; ++g) { const u32x2 ww = *(const u32x2*)(rp + 512 * g); w[2 * g] = ww.x; w[2 * g + 1] = ww.y; }
; #pragma unroll
;                 for (int j = 0; j < 4; ++j) { const f32x2 lo = __builtin_amdgcn_cvt_pk_f32_fp8((int)w[j], false), hi = __builtin_amdgcn_cvt_pk_f32_fp8((int)w[j], true); y[j] += (f32x4){lo.x, lo.y, hi.x, hi.y} * gk; } }
;             const float rstd = rms_rstd(y);
; #pragma unroll
;             for (int j = 0; j < 4; ++j) x[j] = x[j] + Bv[j] * (y[j] * rstd);
	v_cvt_pk_f32_fp8_sdwa v[92:93], v187 src0_sel:WORD_1
	v_pk_fma_f32 v[84:85], v[106:107], v[82:83], v[78:79] op_sel_hi:[0,1,1]
	v_cvt_pk_f32_fp8_e32 v[78:79], v186
	v_pk_fma_f32 v[86:87], v[106:107], v[80:81], v[86:87] op_sel_hi:[0,1,1]
	v_cvt_pk_f32_fp8_sdwa v[82:83], v186 src0_sel:WORD_1
	v_mul_f32_e32 v100, s2, v65
	v_pk_fma_f32 v[80:81], v[106:107], v[78:79], v[94:95] op_sel_hi:[0,1,1]
	v_cvt_pk_f32_fp8_e32 v[78:79], v187
	v_pk_fma_f32 v[82:83], v[106:107], v[82:83], v[102:103] op_sel_hi:[0,1,1]
	v_pk_fma_f32 v[76:77], v[106:107], v[78:79], v[76:77] op_sel_hi:[0,1,1]
	v_pk_fma_f32 v[78:79], v[106:107], v[92:93], v[104:105] op_sel_hi:[0,1,1]
	v_lshl_add_u64 v[92:93], v[70:71], 0, s[4:5]
	s_nop 0
	s_waitcnt vmcnt(4)
	v_cvt_pk_f32_fp8_e32 v[102:103], v188
	v_cvt_pk_f32_fp8_sdwa v[104:105], v188 src0_sel:WORD_1
	v_pk_fma_f32 v[90:91], v[100:101], v[102:103], v[90:91] op_sel_hi:[0,1,1]
	v_cvt_pk_f32_fp8_e32 v[102:103], v189
	v_cvt_pk_f32_fp8_sdwa v[94:95], v189 src0_sel:WORD_1
	v_pk_fma_f32 v[88:89], v[100:101], v[104:105], v[88:89] op_sel_hi:[0,1,1]
	v_pk_fma_f32 v[86:87], v[100:101], v[102:103], v[86:87] op_sel_hi:[0,1,1]
	v_pk_fma_f32 v[84:85], v[100:101], v[94:95], v[84:85] op_sel_hi:[0,1,1]
	s_waitcnt vmcnt(4)
	v_cvt_pk_f32_fp8_e32 v[94:95], v190
	v_cvt_pk_f32_fp8_sdwa v[102:103], v190 src0_sel:WORD_1
	v_pk_fma_f32 v[80:81], v[100:101], v[94:95], v[80:81] op_sel_hi:[0,1,1]
	v_cvt_pk_f32_fp8_e32 v[94:95], v191
	v_cvt_pk_f32_fp8_sdwa v[92:93], v191 src0_sel:WORD_1
	v_pk_fma_f32 v[82:83], v[100:101], v[102:103], v[82:83] op_sel_hi:[0,1,1]
	v_pk_fma_f32 v[76:77], v[100:101], v[94:95], v[76:77] op_sel_hi:[0,1,1]
	v_pk_fma_f32 v[78:79], v[100:101], v[92:93], v[78:79] op_sel_hi:[0,1,1]
	v_pk_mul_f32 v[92:93], v[88:89], v[88:89]
	v_pk_mul_f32 v[94:95], v[90:91], v[90:91]
	s_nop 0
	v_pk_mov_b32 v[100:101], v[94:95], v[92:93] op_sel:[1,0]
	v_mov_b32_e32 v95, v93
	v_pk_add_f32 v[92:93], v[100:101], v[94:95]
	v_pk_mul_f32 v[94:95], v[84:85], v[84:85]
	v_pk_mul_f32 v[100:101], v[86:87], v[86:87]
	v_pk_add_f32 v[92:93], v[92:93], v[92:93] op_sel:[0,1] op_sel_hi:[1,0]
	v_pk_mov_b32 v[102:103], v[100:101], v[94:95] op_sel:[1,0]
	v_mov_b32_e32 v101, v95
	v_pk_add_f32 v[94:95], v[102:103], v[100:101]
	v_mul_f32_e32 v100, v76, v76
	v_mul_f32_e32 v101, v77, v77
	v_pk_add_f32 v[94:95], v[94:95], v[94:95] op_sel:[0,1] op_sel_hi:[1,0]
	v_mov_b32_e32 v93, v100
	v_mov_b32_e32 v95, v101
	v_pk_add_f32 v[92:93], v[92:93], v[94:95]
	v_mul_f32_e32 v94, v81, v81
	v_mul_f32_e32 v100, v83, v83
	v_mul_f32_e32 v102, v78, v78
	v_mul_f32_e32 v103, v79, v79
	v_pk_fma_f32 v[94:95], v[80:81], v[80:81], v[94:95] op_sel_hi:[1,1,0]
	v_pk_fma_f32 v[100:101], v[82:83], v[82:83], v[100:101] op_sel_hi:[1,1,0]
	v_mov_b32_e32 v95, v102
	v_mov_b32_e32 v101, v103
	v_pk_add_f32 v[94:95], v[94:95], v[100:101]
	s_nop 0
	v_pk_add_f32 v[92:93], v[92:93], v[94:95]
	s_nop 0
	v_add_f32_e32 v92, v92, v93
	s_nop 1
	v_add_f32_dpp v92, v92, v92 quad_perm:[1,0,3,2] row_mask:0xf bank_mask:0xf bound_ctrl:1
	s_nop 1
	v_add_f32_dpp v92, v92, v92 quad_perm:[2,3,0,1] row_mask:0xf bank_mask:0xf bound_ctrl:1
	s_nop 1
	v_add_f32_dpp v92, v92, v92 row_half_mirror row_mask:0xf bank_mask:0xf bound_ctrl:1
	s_nop 1
	v_add_f32_dpp v92, v92, v92 row_mirror row_mask:0xf bank_mask:0xf bound_ctrl:1
	s_nop 0
	v_readlane_b32 s2, v92, 16
	v_readlane_b32 s10, v92, 48
	v_readlane_b32 s4, v92, 0
	v_readlane_b32 s5, v92, 32
	v_mov_b32_e32 v92, s2
	v_mov_b32_e32 v93, s10
	v_pk_add_f32 v[92:93], s[4:5], v[92:93]
	s_mov_b64 s[4:5], -1
	v_add_f32_e32 v92, v92, v93
	v_mov_b32_e32 v93, 0x358637bd
	s_nop 0
	v_fmac_f32_e32 v93, 0x3a800000, v92
	v_rsq_f32_e32 v92, v93
	s_nop 0
	v_pk_mul_f32 v[90:91], v[90:91], v[92:93] op_sel_hi:[1,0]
	v_pk_mul_f32 v[88:89], v[88:89], v[92:93] op_sel_hi:[1,0]
	v_pk_mul_f32 v[86:87], v[86:87], v[92:93] op_sel_hi:[1,0]
	v_pk_mul_f32 v[84:85], v[84:85], v[92:93] op_sel_hi:[1,0]
	v_pk_mul_f32 v[80:81], v[80:81], v[92:93] op_sel_hi:[1,0]
	v_pk_mul_f32 v[82:83], v[82:83], v[92:93] op_sel_hi:[1,0]
	v_pk_mul_f32 v[76:77], v[76:77], v[92:93] op_sel_hi:[1,0]
	v_pk_mul_f32 v[78:79], v[78:79], v[92:93] op_sel_hi:[1,0]
	v_pk_fma_f32 v[50:51], v[2:3], v[88:89], v[50:51]
	v_pk_fma_f32 v[48:49], v[0:1], v[90:91], v[48:49]
	v_pk_fma_f32 v[54:55], v[6:7], v[84:85], v[54:55]
	v_pk_fma_f32 v[52:53], v[4:5], v[86:87], v[52:53]
	v_pk_fma_f32 v[58:59], v[10:11], v[82:83], v[58:59]
	v_pk_fma_f32 v[56:57], v[8:9], v[80:81], v[56:57]
	v_pk_fma_f32 v[62:63], v[14:15], v[78:79], v[62:63]
	v_pk_fma_f32 v[60:61], v[12:13], v[76:77], v[60:61]
	s_cbranch_vccz .LBB0_1397
	s_andn2_b64 vcc, exec, s[4:5]
	s_cbranch_vccnz .LBB0_1390
	s_branch .LBB0_1398
